# baseline (speedup 1.0000x reference)
_Z10pre_kernelPKfS0_S0_S0_S0_S0_S0_S0_S0_S0_S0_PtPfS0_S0_S0_S0_S0_S0_S2_S2_S2_S0_S0_S0_S1_:
	s_cmpk_lt_u32 s2, 64
	s_cbranch_scc1 .Lpre_map_done
	s_cmpk_lt_u32 s2, 0x100
	s_cbranch_scc0 .Lpre_map_hi
	s_addk_i32 s2, 0x6d
	s_branch .Lpre_map_done
.Lpre_map_hi:
	s_cmpk_lt_u32 s2, 0x16d
	s_cbranch_scc0 .Lpre_map_done
	s_sub_u32 s2, s2, 0xc0
.Lpre_map_done:
	s_cmpk_lt_u32 s2, 0x80
	s_cbranch_scc1 .Lpre_roleA_new
	s_cmpk_lt_u32 s2, 0xa0
	s_cbranch_scc1 .Lpre_roleBC
	s_cmpk_lg_u32 s2, 0xa0
	s_cbranch_scc1 .Lpre_not160
	s_endpgm
